# PEER tail round on waves 0 and 5 of every workgroup (two different SIMDs under either wave placement)
# speedup vs baseline: 1.0189x; 1.0011x over previous
.LBB0_719:
	s_lshl_b32 s6, s33, 3
	s_add_i32 s6, s6, s88
	s_cmpk_lt_i32 s6, 0x4000
	s_cbranch_scc1 .Lpe_notail
	s_cmpk_lg_u32 s33, 0x100
	s_cbranch_scc1 .Lpe_notail
	s_and_b32 s8, s6, 7
	s_cmp_eq_u32 s8, 1
	s_cselect_b32 s8, 7, s8
	s_cmp_eq_u32 s8, 5
	s_cselect_b32 s8, 1, s8
	s_sub_i32 s9, s6, 0x4000
	s_lshr_b32 s9, s9, 3
	s_lshl_b32 s9, s9, 1
	s_add_i32 s9, s9, s8
	s_addk_i32 s9, 0x4000
	s_cmp_lt_u32 s8, 2
	s_cselect_b32 s6, s9, 0x7ffffff0
